# baseline (speedup 1.0000x reference)
.Lstag_done_p1:
	s_mov_b32 s66, s2
	s_load_dwordx2 s[64:65], s[0:1], 0x0
	v_lshrrev_b32_e32 v112, 6, v0
	v_bfe_u32 v113, v0, 2, 4
	v_lshl_add_u32 v112, v112, 7, v113
	v_lshlrev_b32_e32 v113, 4, v0
	v_and_b32_e32 v113, 48, v113
	v_lshl_add_u32 v112, v112, 9, v113
	s_lshr_b32 s22, s2, 3
	s_sub_i32 s22, 0xbf, s22
	s_and_b32 s2, s2, 7
	s_lshl_b32 s22, s22, 3
	s_or_b32 s2, s2, s22
	s_ashr_i32 s15, s2, 3
	s_mul_hi_i32 s14, s15, 0x55555556
	s_lshr_b32 s12, s14, 31
	s_add_i32 s14, s14, s12
	s_mul_i32 s16, s14, 0x3fffffd
	s_add_i32 s16, s16, s15
	s_lshl_b32 s15, s16, 6
	s_lshl_b32 s16, s2, 5
	s_and_b32 s16, s16, 32
	s_or_b32 s15, s15, s16
	s_bfe_u32 s16, s2, 0x20001
	s_mul_i32 s2, s16, 0xc0
	s_lshl_b32 s12, s14, 1
	s_add_i32 s17, s15, s2
	s_load_dwordx8 s[4:11], s[0:1], 0x0
	s_and_b32 s12, s12, -16
	s_lshl_b32 s13, s14, 4
	s_and_b32 s13, s13, 0x70
	s_mov_b32 s3, 0
	v_mov_b32_e32 v32, 0
	v_lshrrev_b32_e32 v78, 6, v0
	v_bfe_u32 v65, v0, 2, 4
	v_lshlrev_b32_e32 v1, 4, v0
	v_and_b32_e32 v30, 48, v1
	v_lshl_add_u32 v1, v78, 7, v65
	v_lshl_add_u32 v1, v1, 9, v30
	s_lshl_b32 s18, s17, 7
	s_add_i32 s18, s18, s12
	s_lshl_b32 s18, s18, 9
	s_lshl_b32 s2, s13, 2
	s_add_i32 s18, s18, s2
	s_waitcnt lgkmcnt(0)
	s_add_u32 s20, s4, s18
	s_addc_u32 s21, s5, 0
	s_add_u32 s22, s20, 0x40000
	s_addc_u32 s23, s21, 0
	s_add_u32 s24, s22, 0x40000
	s_addc_u32 s25, s23, 0
	s_add_u32 s26, s24, 0x40000
	s_addc_u32 s27, s25, 0
	s_add_u32 s28, s26, 0x40000
	s_addc_u32 s29, s27, 0
	s_add_u32 s30, s28, 0x40000
	s_addc_u32 s31, s29, 0
	s_add_u32 s32, s30, 0x40000
	s_addc_u32 s33, s31, 0
	s_add_u32 s34, s32, 0x40000
	s_addc_u32 s35, s33, 0
	global_load_dwordx4 v[2:5], v1, s[34:35]
	global_load_dwordx4 v[6:9], v1, s[32:33]
	global_load_dwordx4 v[10:13], v1, s[30:31]
	global_load_dwordx4 v[14:17], v1, s[28:29]
	global_load_dwordx4 v[18:21], v1, s[26:27]
	global_load_dwordx4 v[22:25], v1, s[24:25]
	v_bfe_u32 v103, v0, 5, 1
	v_lshrrev_b32_e32 v33, 2, v0
	global_load_dwordx4 v[66:69], v1, s[22:23]
	global_load_dwordx4 v[74:77], v1, s[20:21]
	v_lshlrev_b32_e32 v104, 1, v78
	v_and_b32_e32 v27, 3, v0
	v_lshrrev_b32_e32 v28, 1, v0
	v_and_or_b32 v59, v33, 1, v104
	v_and_or_b32 v105, v28, 12, v27
	v_lshlrev_b32_e32 v28, 4, v103
	v_mov_b32_e32 v29, v32
	v_lshl_add_u64 v[56:57], s[6:7], 0, v[28:29]
	v_or_b32_e32 v27, s13, v59
	v_or_b32_e32 v28, s12, v105
	s_lshl_b32 s4, s16, 16
	v_lshl_add_u32 v31, v27, 7, v28
	s_or_b32 s2, s4, 0x4000
	v_add_u32_e32 v27, 0x400, v31
	s_or_b32 s5, s4, 0xc000
	v_add_u32_e32 v28, s2, v27
	v_and_b32_e32 v1, 31, v0
	v_ashrrev_i32_e32 v29, 31, v28
	v_add_u32_e32 v34, s5, v27
	v_or_b32_e32 v26, s15, v1
	v_lshlrev_b64 v[28:29], 5, v[28:29]
	v_ashrrev_i32_e32 v35, 31, v34
	v_lshl_add_u64 v[28:29], v[56:57], 0, v[28:29]
	v_lshlrev_b64 v[34:35], 5, v[34:35]
	v_lshl_or_b32 v58, v26, 1, v103
	v_lshl_add_u64 v[34:35], v[56:57], 0, v[34:35]
	global_load_dwordx4 v[36:39], v[28:29], off
	global_load_dwordx4 v[40:43], v[34:35], off
	v_add_u32_e32 v28, 0x180, v58
	v_ashrrev_i32_e32 v29, 31, v28
	v_add_u32_e32 v34, 0x480, v58
	v_lshl_add_u64 v[28:29], v[28:29], 4, s[8:9]
	v_ashrrev_i32_e32 v35, 31, v34
	v_ashrrev_i32_e32 v27, 31, v26
	v_lshl_add_u64 v[34:35], v[34:35], 4, s[8:9]
	global_load_dwordx4 v[44:47], v[28:29], off
	global_load_dwordx4 v[48:51], v[34:35], off
	v_lshl_add_u64 v[60:61], v[26:27], 2, s[10:11]
	v_add_u32_e32 v26, s5, v31
	v_add_u32_e32 v28, s2, v31
	v_ashrrev_i32_e32 v27, 31, v26
	v_ashrrev_i32_e32 v29, 31, v28
	v_lshlrev_b64 v[26:27], 5, v[26:27]
	v_lshlrev_b64 v[28:29], 5, v[28:29]
	global_load_dword v62, v[60:61], off offset:768
	global_load_dword v64, v[60:61], off offset:2304
	v_lshl_add_u64 v[26:27], v[56:57], 0, v[26:27]
	v_lshl_add_u64 v[28:29], v[56:57], 0, v[28:29]
	global_load_dwordx4 v[52:55], v[26:27], off
	s_nop 0
	global_load_dwordx4 v[26:29], v[28:29], off
	s_load_dwordx2 s[0:1], s[0:1], 0x28
	v_and_b32_e32 v0, 63, v0
	v_bfrev_b32_e32 v31, 60
	v_cmp_gt_u32_e32 vcc, 32, v0
	v_mul_u32_u24_e32 v102, 0x410, v1
	v_lshlrev_b32_e32 v0, 2, v1
	v_mov_b32_e32 v1, v32
	v_cndmask_b32_e64 v34, v31, 0, vcc
	s_waitcnt lgkmcnt(0)
	v_lshl_add_u64 v[72:73], s[0:1], 0, v[0:1]
	v_mul_u32_u24_e32 v0, 0x410, v78
	v_lshlrev_b32_e32 v1, 6, v65
	v_add3_u32 v1, v0, v1, v30
	s_mul_i32 s16, s16, 24
	s_lshr_b32 s0, s15, 5
	s_waitcnt vmcnt(8)
	ds_write_b128 v1, v[74:77]
	ds_write_b128 v1, v[66:69] offset:4160
	ds_write_b128 v1, v[22:25] offset:8320
	ds_write_b128 v1, v[18:21] offset:12480
	ds_write_b128 v1, v[14:17] offset:16640
	ds_write_b128 v1, v[10:13] offset:20800
	ds_write_b128 v1, v[6:9] offset:24960
	ds_write_b128 v1, v[2:5] offset:29120
	s_add_i32 s0, s0, s16
	s_waitcnt lgkmcnt(0)
	s_barrier
	s_lshl_b32 s2, s0, 10
	v_mov_b32_e32 v33, v32
	v_mov_b32_e32 v35, v32
	v_lshl_or_b32 v106, v103, 2, v102
	s_add_i32 s5, s2, 0x4800
	v_or_b32_e32 v107, s13, v103
	s_ashr_i32 s6, s14, 3
	s_add_i32 s7, s2, 0x1800
	s_mov_b64 s[0:1], -1
	s_mov_b32 s10, 0x7f61b1e6
	s_mov_b32 s11, 0x42800000
	s_waitcnt vmcnt(3)
	v_mov_b32_e32 v63, v62
	s_waitcnt vmcnt(2)
	v_mov_b32_e32 v65, v64
	s_waitcnt vmcnt(0)
	s_branch .LBB2_3

.LBB2_9:
	s_cmp_lg_u32 s7, 0
	s_cbranch_scc1 .Lp1_nopf
	s_cmpk_gt_i32 s66, 0x1ff
	s_cbranch_scc1 .Lp1_nopf
	s_add_i32 s43, s66, 0x400
	s_lshr_b32 s60, s43, 3
	s_sub_i32 s60, 0xbf, s60
	s_and_b32 s61, s43, 7
	s_lshl_b32 s60, s60, 3
	s_or_b32 s43, s61, s60
	s_ashr_i32 s60, s43, 3
	s_mul_hi_i32 s61, s60, 0x55555556
	s_lshr_b32 s62, s61, 31
	s_add_i32 s61, s61, s62
	s_mul_i32 s62, s61, 0x3fffffd
	s_add_i32 s62, s62, s60
	s_lshl_b32 s62, s62, 6
	s_lshl_b32 s63, s43, 5
	s_and_b32 s63, s63, 32
	s_or_b32 s62, s62, s63
	s_bfe_u32 s63, s43, 0x20001
	s_mul_i32 s63, s63, 0xc0
	s_add_i32 s62, s62, s63
	s_lshl_b32 s62, s62, 7
	s_lshl_b32 s63, s61, 1
	s_and_b32 s63, s63, -16
	s_add_i32 s62, s62, s63
	s_lshl_b32 s62, s62, 9
	s_lshl_b32 s63, s61, 4
	s_and_b32 s63, s63, 0x70
	s_lshl_b32 s63, s63, 2
	s_add_i32 s62, s62, s63
	s_add_u32 s44, s64, s62
	s_addc_u32 s45, s65, 0
	s_add_u32 s46, s44, 0x40000
	s_addc_u32 s47, s45, 0
	s_add_u32 s48, s46, 0x40000
	s_addc_u32 s49, s47, 0
	s_add_u32 s50, s48, 0x40000
	s_addc_u32 s51, s49, 0
	s_add_u32 s52, s50, 0x40000
	s_addc_u32 s53, s51, 0
	s_add_u32 s54, s52, 0x40000
	s_addc_u32 s55, s53, 0
	s_add_u32 s56, s54, 0x40000
	s_addc_u32 s57, s55, 0
	s_add_u32 s58, s56, 0x40000
	s_addc_u32 s59, s57, 0
	global_load_dwordx4 v[116:119], v112, s[44:45]
	global_load_dwordx4 v[116:119], v112, s[46:47]
	global_load_dwordx4 v[116:119], v112, s[48:49]
	global_load_dwordx4 v[116:119], v112, s[50:51]
	global_load_dwordx4 v[116:119], v112, s[52:53]
	global_load_dwordx4 v[116:119], v112, s[54:55]
	global_load_dwordx4 v[116:119], v112, s[56:57]
	global_load_dwordx4 v[116:119], v112, s[58:59]

	.amdhsa_kernel _Z11scan_kernelILi1ELi1536ELi4EEvPKfPKDF16_S3_S1_S1_PDv2_DF16_S3_Pf
		.amdhsa_group_segment_fixed_size 33280
		.amdhsa_private_segment_fixed_size 0
		.amdhsa_kernarg_size 64
		.amdhsa_user_sgpr_count 2
		.amdhsa_user_sgpr_dispatch_ptr 0
		.amdhsa_user_sgpr_queue_ptr 0
		.amdhsa_user_sgpr_kernarg_segment_ptr 1
		.amdhsa_user_sgpr_dispatch_id 0
		.amdhsa_user_sgpr_kernarg_preload_length 0
		.amdhsa_user_sgpr_kernarg_preload_offset 0
		.amdhsa_user_sgpr_private_segment_size 0
		.amdhsa_uses_dynamic_stack 0
		.amdhsa_enable_private_segment 0
		.amdhsa_system_sgpr_workgroup_id_x 1
		.amdhsa_system_sgpr_workgroup_id_y 0
		.amdhsa_system_sgpr_workgroup_id_z 0
		.amdhsa_system_sgpr_workgroup_info 0
		.amdhsa_system_vgpr_workitem_id 0
		.amdhsa_next_free_vgpr 120
		.amdhsa_next_free_sgpr 96
		.amdhsa_accum_offset 120
		.amdhsa_reserve_vcc 1
		.amdhsa_float_round_mode_32 0
		.amdhsa_float_round_mode_16_64 0
		.amdhsa_float_denorm_mode_32 3
		.amdhsa_float_denorm_mode_16_64 3
		.amdhsa_dx10_clamp 1
		.amdhsa_ieee_mode 1
		.amdhsa_fp16_overflow 0
		.amdhsa_tg_split 0
		.amdhsa_exception_fp_ieee_invalid_op 0
		.amdhsa_exception_fp_denorm_src 0
		.amdhsa_exception_fp_ieee_div_zero 0
		.amdhsa_exception_fp_ieee_overflow 0
		.amdhsa_exception_fp_ieee_underflow 0
		.amdhsa_exception_fp_ieee_inexact 0
		.amdhsa_exception_int_div_zero 0
	.end_amdhsa_kernel

amdhsa.kernels:
  - .agpr_count:     0
    .args:
      - .actual_access:  read_only
        .address_space:  global
        .offset:         0
        .size:           8
        .value_kind:     global_buffer
      - .actual_access:  read_only
        .address_space:  global
        .offset:         8
        .size:           8
        .value_kind:     global_buffer
      - .actual_access:  read_only
        .address_space:  global
        .offset:         16
        .size:           8
        .value_kind:     global_buffer
      - .actual_access:  read_only
        .address_space:  global
        .offset:         24
        .size:           8
        .value_kind:     global_buffer
      - .actual_access:  read_only
        .address_space:  global
        .offset:         32
        .size:           8
        .value_kind:     global_buffer
      - .actual_access:  read_only
        .address_space:  global
        .offset:         40
        .size:           8
        .value_kind:     global_buffer
      - .actual_access:  write_only
        .address_space:  global
        .offset:         48
        .size:           8
        .value_kind:     global_buffer
      - .actual_access:  write_only
        .address_space:  global
        .offset:         56
        .size:           8
        .value_kind:     global_buffer
      - .actual_access:  write_only
        .address_space:  global
        .offset:         64
        .size:           8
        .value_kind:     global_buffer
      - .actual_access:  write_only
        .address_space:  global
        .offset:         72
        .size:           8
        .value_kind:     global_buffer
    .group_segment_fixed_size: 65536
    .kernarg_segment_align: 8
    .kernarg_segment_size: 80
    .language:       OpenCL C
    .language_version:
      - 2
      - 0
    .max_flat_workgroup_size: 256
    .name:           _Z11proj_kernelPKfS0_S0_S0_S0_S0_PDF16_S1_PfS2_
    .private_segment_fixed_size: 0
    .sgpr_count:     22
    .sgpr_spill_count: 0
    .symbol:         _Z11proj_kernelPKfS0_S0_S0_S0_S0_PDF16_S1_PfS2_.kd
    .uniform_work_group_size: 1
    .uses_dynamic_stack: false
    .vgpr_count:     200
    .vgpr_spill_count: 0
    .wavefront_size: 64
  - .agpr_count:     0
    .args:
      - .actual_access:  read_only
        .address_space:  global
        .offset:         0
        .size:           8
        .value_kind:     global_buffer
      - .actual_access:  write_only
        .address_space:  global
        .offset:         8
        .size:           8
        .value_kind:     global_buffer
    .group_segment_fixed_size: 12672
    .kernarg_segment_align: 8
    .kernarg_segment_size: 16
    .language:       OpenCL C
    .language_version:
      - 2
      - 0
    .max_flat_workgroup_size: 1024
    .name:           _Z12carry_kernelPKDv2_DF16_PDF16_
    .private_segment_fixed_size: 0
    .sgpr_count:     16
    .sgpr_spill_count: 0
    .symbol:         _Z12carry_kernelPKDv2_DF16_PDF16_.kd
    .uniform_work_group_size: 1
    .uses_dynamic_stack: false
    .vgpr_count:     90
    .vgpr_spill_count: 0
    .wavefront_size: 64
  - .agpr_count:     0
    .args:
      - .actual_access:  read_only
        .address_space:  global
        .offset:         0
        .size:           8
        .value_kind:     global_buffer
      - .actual_access:  read_only
        .address_space:  global
        .offset:         8
        .size:           8
        .value_kind:     global_buffer
      - .actual_access:  read_only
        .address_space:  global
        .offset:         16
        .size:           8
        .value_kind:     global_buffer
      - .actual_access:  read_only
        .address_space:  global
        .offset:         24
        .size:           8
        .value_kind:     global_buffer
      - .actual_access:  read_only
        .address_space:  global
        .offset:         32
        .size:           8
        .value_kind:     global_buffer
      - .actual_access:  write_only
        .address_space:  global
        .offset:         40
        .size:           8
        .value_kind:     global_buffer
      - .actual_access:  read_only
        .address_space:  global
        .offset:         48
        .size:           8
        .value_kind:     global_buffer
      - .actual_access:  read_only
        .address_space:  global
        .offset:         56
        .size:           8
        .value_kind:     global_buffer
    .group_segment_fixed_size: 33280
    .kernarg_segment_align: 8
    .kernarg_segment_size: 64
    .language:       OpenCL C
    .language_version:
      - 2
      - 0
    .max_flat_workgroup_size: 256
    .name:           _Z11scan_kernelILi1ELi1536ELi4EEvPKfPKDF16_S3_S1_S1_PDv2_DF16_S3_Pf
    .private_segment_fixed_size: 0
    .sgpr_count:     24
    .sgpr_spill_count: 0
    .symbol:         _Z11scan_kernelILi1ELi1536ELi4EEvPKfPKDF16_S3_S1_S1_PDv2_DF16_S3_Pf.kd
    .uniform_work_group_size: 1
    .uses_dynamic_stack: false
    .vgpr_count:     120
    .vgpr_spill_count: 0
    .wavefront_size: 64
  - .agpr_count:     0
    .args:
      - .actual_access:  read_only
        .address_space:  global
        .offset:         0
        .size:           8
        .value_kind:     global_buffer
      - .actual_access:  read_only
        .address_space:  global
        .offset:         8
        .size:           8
        .value_kind:     global_buffer
      - .actual_access:  read_only
        .address_space:  global
        .offset:         16
        .size:           8
        .value_kind:     global_buffer
      - .actual_access:  read_only
        .address_space:  global
        .offset:         24
        .size:           8
        .value_kind:     global_buffer
      - .actual_access:  read_only
        .address_space:  global
        .offset:         32
        .size:           8
        .value_kind:     global_buffer
      - .actual_access:  read_only
        .address_space:  global
        .offset:         40
        .size:           8
        .value_kind:     global_buffer
      - .actual_access:  read_only
        .address_space:  global
        .offset:         48
        .size:           8
        .value_kind:     global_buffer
      - .actual_access:  write_only
        .address_space:  global
        .offset:         56
        .size:           8
        .value_kind:     global_buffer
    .group_segment_fixed_size: 50176
    .kernarg_segment_align: 8
    .kernarg_segment_size: 64
    .language:       OpenCL C
    .language_version:
      - 2
      - 0
    .max_flat_workgroup_size: 256
    .name:           _Z11scan_kernelILi3ELi1536ELi3EEvPKfPKDF16_S3_S1_S1_PDv2_DF16_S3_Pf
    .private_segment_fixed_size: 0
    .sgpr_count:     28
    .sgpr_spill_count: 0
    .symbol:         _Z11scan_kernelILi3ELi1536ELi3EEvPKfPKDF16_S3_S1_S1_PDv2_DF16_S3_Pf.kd
    .uniform_work_group_size: 1
    .uses_dynamic_stack: false
    .vgpr_count:     168
    .vgpr_spill_count: 0
    .wavefront_size: 64
